# speedup vs baseline: 1.0323x; 1.0290x over previous
.Lno_anc:
	s_or_b64 exec, exec, s[8:9]
	v_mov_b32_e32 v7, 0x80
	s_waitcnt vmcnt(0)
	s_sleep 48
	v_cmp_ne_u32_e64 s[4:5], 0, v12
	s_nop 1
	v_cndmask_b32_e64 v8, 0, 1, s[4:5]
	v_cmp_eq_u32_e64 s[4:5], 0, v13
	s_nop 1
	v_cndmask_b32_e64 v9, 2, 0, s[4:5]
	v_cmp_eq_u32_e64 s[4:5], 0, v14
	v_or_b32_e32 v8, v9, v8
	s_nop 0
	v_cndmask_b32_e64 v12, 4, 0, s[4:5]
	v_cmp_eq_u32_e64 s[4:5], 0, v15
	s_nop 1
	v_cndmask_b32_e64 v13, 8, 0, s[4:5]
	v_cmp_eq_u32_e64 s[4:5], 0, v16
	v_or3_b32 v8, v8, v12, v13
	s_nop 0
	v_cndmask_b32_e64 v14, 16, 0, s[4:5]
	v_cmp_eq_u32_e64 s[4:5], 0, v17
	s_nop 1
	v_cndmask_b32_e64 v15, 32, 0, s[4:5]
	v_cmp_eq_u32_e64 s[4:5], 0, v18
	s_nop 1
	v_cndmask_b32_e64 v16, 64, 0, s[4:5]
	v_cmp_eq_u32_e64 s[4:5], 0, v19
	s_nop 1
	v_cndmask_b32_e64 v7, v7, 0, s[4:5]
	v_or_b32_e32 v7, v16, v7
	v_or3_b32 v9, v7, v15, v14
	v_or_b32_e32 v7, v9, v8
	v_bcnt_u32_b32 v8, v8, 0
	v_bcnt_u32_b32 v9, v9, 0
	v_lshl_or_b32 v9, v9, 16, v8
	v_cmp_ne_u32_e64 s[4:5], 0, v7
	s_nop 0
	v_add_u32_dpp v8, v9, v9 row_shr:1 row_mask:0xf bank_mask:0xf bound_ctrl:1
	s_nop 1
	v_add_u32_dpp v8, v8, v8 row_shr:2 row_mask:0xf bank_mask:0xf bound_ctrl:1
	s_nop 1
	v_add_u32_dpp v8, v8, v8 row_shr:4 row_mask:0xf bank_mask:0xf bound_ctrl:1
	s_nop 1
	v_add_u32_dpp v12, v8, v8 row_shr:8 row_mask:0xf bank_mask:0xf bound_ctrl:1
	s_nop 1
	v_add_u32_dpp v12, v12, v12 row_bcast:15 row_mask:0xa bank_mask:0xf
	s_nop 1
	v_add_u32_dpp v12, v12, v12 row_bcast:31 row_mask:0xc bank_mask:0xf
	s_nop 0
	v_readlane_b32 s14, v12, 63
	s_and_b32 s3, s14, 0xffff
	s_and_saveexec_b64 s[10:11], s[4:5]
	s_cbranch_execz .LBB0_5
	v_sub_u32_e32 v12, v12, v9
	v_lshlrev_b32_e32 v8, 10, v1
	v_add_u32_sdwa v9, sext(v12), s3 dst_sel:DWORD dst_unused:UNUSED_PAD src0_sel:WORD_1 src1_sel:DWORD
	v_and_b32_e32 v12, 0xffff, v12
	v_lshlrev_b32_e32 v13, 2, v10
	s_mov_b64 s[12:13], 0
	v_mov_b32_e32 v14, 0x100
